# P4b merge epilogue: running sum of row groups 0-4 kept on chip (VGPRs + 8 KB spare LDS), borrowed constant registers re-materialised at P5 start
# speedup vs baseline: 1.0352x; 1.0064x over previous
.LBB0_802:
	s_cmp_gt_u32 s0, 7
	s_cselect_b64 s[34:35], -1, 0
	v_lshl_add_u32 v222, s86, 6, v213
	v_lshlrev_b32_e32 v222, 4, v222
	v_add_u32_e32 v222, 0x200c0, v222
	s_lshl_b32 s1, s0, 8
	s_and_b32 s26, s1, 0xfffffc00
	s_ashr_i32 s27, s26, 31
	s_and_b32 s19, s1, 0x300
	s_lshl_b64 s[30:31], s[26:27], 2
	v_or_b32_e32 v0, s19, v191
	s_add_u32 s30, s56, s30
	v_lshl_add_u32 v162, s28, 8, v190
	v_mov_b64_e32 v[18:19], s[12:13]
	s_movk_i32 s66, 0x1800
	s_addc_u32 s31, s57, s31
	v_lshlrev_b32_e32 v6, 2, v0
	v_mad_i64_i32 v[18:19], s[28:29], v162, s66, v[18:19]
	s_nop 15
	s_nop 3
	global_load_dwordx4 v[10:13], v6, s[30:31] offset:16
	global_load_dwordx4 v[14:17], v6, s[30:31]
	global_load_dwordx4 v[2:5], v6, s[30:31] offset:528
	s_nop 0
	global_load_dwordx4 v[6:9], v6, s[30:31] offset:512
	v_lshl_add_u64 v[18:19], s[26:27], 1, v[18:19]
	v_lshlrev_b32_e32 v0, 1, v0
	v_lshl_add_u64 v[18:19], v[18:19], 0, v[0:1]
	global_load_dwordx4 v[30:33], v[18:19], off
	v_ashrrev_i32_e32 v163, 31, v162
	s_cmp_gt_u32 s0, 3
	s_cselect_b64 s[28:29], -1, 0
	v_lshlrev_b64 v[20:21], 11, v[162:163]
	v_readlane_b32 s68, v253, 41
	v_lshl_add_u64 v[178:179], s[10:11], 0, v[20:21]
	v_mov_b32_e32 v176, 0
	s_and_b64 vcc, exec, s[28:29]
	v_mov_b32_e32 v182, 0
	v_mov_b32_e32 v183, 0
	v_mov_b32_e32 v180, 0
	v_mov_b32_e32 v181, 0
	v_readlane_b32 s69, v253, 42
	v_readlane_b32 s67, v253, 52
	s_cbranch_vccz .LBB0_804
	v_lshl_add_u64 v[20:21], v[178:179], 0, v[0:1]
	v_mov_b32_e32 v182, v224
	v_mov_b32_e32 v183, v225
	v_mov_b32_e32 v180, v226
	v_mov_b32_e32 v181, v227

.LBB0_812:
	s_nop 0
	global_load_dwordx4 v[22:25], v[22:23], off offset:256
	s_and_b64 vcc, exec, s[0:1]
	v_mov_b32_e32 v149, 0
	v_mov_b32_e32 v146, 0
	v_mov_b32_e32 v147, 0
	s_cbranch_vccnz .LBB0_814
	v_lshl_add_u64 v[146:147], v[150:151], 0, v[0:1]
	v_mov_b32_e32 v148, v248
	v_mov_b32_e32 v149, v249
	s_nop 0
	v_mov_b32_e32 v146, v216
	v_mov_b32_e32 v147, v217
.LBB0_814:
	v_add_f32_e32 v142, v142, v14
	v_add_f32_e32 v143, v143, v15
	v_mul_f32_e32 v142, 0xbfb8aa3b, v142
	v_mul_f32_e32 v143, 0xbfb8aa3b, v143
	v_exp_f32_e32 v142, v142
	v_exp_f32_e32 v143, v143
	s_waitcnt vmcnt(5)
	v_lshlrev_b32_e32 v156, 16, v26
	v_and_b32_e32 v157, 0xffff0000, v26
	v_add_f32_e32 v26, v144, v16
	v_mul_f32_e32 v26, 0xbfb8aa3b, v26
	v_add_f32_e32 v144, v145, v17
	v_add_f32_e32 v142, 1.0, v142
	v_add_f32_e32 v143, 1.0, v143
	v_exp_f32_e32 v26, v26
	v_mul_f32_e32 v144, 0xbfb8aa3b, v144
	v_rcp_f32_e32 v142, v142
	v_rcp_f32_e32 v143, v143
	v_exp_f32_e32 v145, v144
	v_add_f32_e32 v138, v138, v10
	v_lshlrev_b32_e32 v158, 16, v172
	v_and_b32_e32 v159, 0xffff0000, v172
	v_add_f32_e32 v26, 1.0, v26
	v_mul_f32_e32 v138, 0xbfb8aa3b, v138
	v_pk_fma_f32 v[142:143], v[142:143], v[156:157], v[158:159]
	v_rcp_f32_e32 v144, v26
	v_add_f32_e32 v26, 1.0, v145
	v_exp_f32_e32 v158, v138
	v_add_f32_e32 v138, v139, v11
	v_rcp_f32_e32 v145, v26
	v_mul_f32_e32 v138, 0xbfb8aa3b, v138
	v_exp_f32_e32 v159, v138
	v_lshlrev_b32_e32 v26, 16, v27
	v_and_b32_e32 v27, 0xffff0000, v27
	v_lshlrev_b32_e32 v156, 16, v173
	v_and_b32_e32 v157, 0xffff0000, v173
	v_pk_fma_f32 v[138:139], v[144:145], v[26:27], v[156:157]
	v_lshlrev_b32_e32 v144, 16, v28
	v_and_b32_e32 v145, 0xffff0000, v28
	v_add_f32_e32 v28, v140, v12
	v_add_f32_e32 v140, v141, v13
	v_add_f32_e32 v26, 1.0, v158
	v_add_f32_e32 v27, 1.0, v159
	v_mul_f32_e32 v28, 0xbfb8aa3b, v28
	v_mul_f32_e32 v140, 0xbfb8aa3b, v140
	v_rcp_f32_e32 v26, v26
	v_rcp_f32_e32 v27, v27
	v_exp_f32_e32 v28, v28
	v_exp_f32_e32 v158, v140
	v_lshlrev_b32_e32 v156, 16, v170
	v_and_b32_e32 v157, 0xffff0000, v170
	v_pk_fma_f32 v[140:141], v[26:27], v[144:145], v[156:157]
	v_add_f32_e32 v26, 1.0, v28
	v_add_f32_e32 v27, 1.0, v158
	v_rcp_f32_e32 v26, v26
	v_rcp_f32_e32 v27, v27
	v_add_f32_e32 v134, v134, v6
	v_add_f32_e32 v135, v135, v7
	v_lshlrev_b32_e32 v28, 16, v29
	v_and_b32_e32 v29, 0xffff0000, v29
	v_lshlrev_b32_e32 v144, 16, v171
	v_and_b32_e32 v145, 0xffff0000, v171
	v_mul_f32_e32 v134, 0xbfb8aa3b, v134
	v_mul_f32_e32 v135, 0xbfb8aa3b, v135
	v_pk_fma_f32 v[144:145], v[26:27], v[28:29], v[144:145]
	v_exp_f32_e32 v134, v134
	v_exp_f32_e32 v135, v135
	v_cvt_pk_bf16_f32 v26, v142, v143
	v_cvt_pk_bf16_f32 v27, v138, v139
	v_cvt_pk_bf16_f32 v28, v140, v141
	v_cvt_pk_bf16_f32 v29, v144, v145
	v_lshl_add_u64 v[138:139], v[168:169], 0, v[0:1]
	v_mov_b32_e32 v232, v26
	v_mov_b32_e32 v233, v27
	v_mov_b32_e32 v234, v28
	v_mov_b32_e32 v235, v29
	s_mov_b64 exec, s[34:35]
	global_store_dwordx4 v[138:139], v[26:29], off
	s_mov_b64 exec, -1
	v_add_f32_e32 v130, v130, v2
	v_add_f32_e32 v131, v131, v3
	s_waitcnt vmcnt(5)
	v_lshlrev_b32_e32 v28, 16, v18
	v_and_b32_e32 v29, 0xffff0000, v18
	v_add_f32_e32 v18, v136, v8
	v_mul_f32_e32 v18, 0xbfb8aa3b, v18
	v_add_f32_e32 v136, v137, v9
	v_add_f32_e32 v26, 1.0, v134
	v_add_f32_e32 v27, 1.0, v135
	v_exp_f32_e32 v18, v18
	v_mul_f32_e32 v136, 0xbfb8aa3b, v136
	v_rcp_f32_e32 v26, v26
	v_rcp_f32_e32 v27, v27
	v_exp_f32_e32 v136, v136
	v_lshlrev_b32_e32 v134, 16, v166
	v_and_b32_e32 v135, 0xffff0000, v166
	v_add_f32_e32 v18, 1.0, v18
	v_pk_fma_f32 v[26:27], v[26:27], v[28:29], v[134:135]
	v_rcp_f32_e32 v28, v18
	v_add_f32_e32 v18, 1.0, v136
	v_mul_f32_e32 v130, 0xbfb8aa3b, v130
	v_mul_f32_e32 v131, 0xbfb8aa3b, v131
	v_rcp_f32_e32 v29, v18
	v_exp_f32_e32 v130, v130
	v_exp_f32_e32 v131, v131
	v_lshlrev_b32_e32 v18, 16, v19
	v_and_b32_e32 v19, 0xffff0000, v19
	v_lshlrev_b32_e32 v134, 16, v167
	v_and_b32_e32 v135, 0xffff0000, v167
	v_pk_fma_f32 v[28:29], v[28:29], v[18:19], v[134:135]
	v_add_f32_e32 v18, 1.0, v130
	v_add_f32_e32 v19, 1.0, v131
	v_lshlrev_b32_e32 v130, 16, v20
	v_and_b32_e32 v131, 0xffff0000, v20
	v_add_f32_e32 v20, v132, v4
	v_add_f32_e32 v132, v133, v5
	v_mul_f32_e32 v20, 0xbfb8aa3b, v20
	v_mul_f32_e32 v132, 0xbfb8aa3b, v132
	v_rcp_f32_e32 v18, v18
	v_rcp_f32_e32 v19, v19
	v_exp_f32_e32 v20, v20
	v_exp_f32_e32 v132, v132
	v_lshlrev_b32_e32 v134, 16, v164
	v_and_b32_e32 v135, 0xffff0000, v164
	v_pk_fma_f32 v[130:131], v[18:19], v[130:131], v[134:135]
	v_add_f32_e32 v18, 1.0, v20
	v_add_f32_e32 v19, 1.0, v132
	v_rcp_f32_e32 v18, v18
	v_rcp_f32_e32 v19, v19
	v_lshlrev_b32_e32 v20, 16, v21
	v_and_b32_e32 v21, 0xffff0000, v21
	v_lshlrev_b32_e32 v132, 16, v165
	v_and_b32_e32 v133, 0xffff0000, v165
	v_pk_fma_f32 v[132:133], v[18:19], v[20:21], v[132:133]
	v_cvt_pk_bf16_f32 v18, v26, v27
	v_cvt_pk_bf16_f32 v19, v28, v29
	v_cvt_pk_bf16_f32 v20, v130, v131
	v_cvt_pk_bf16_f32 v21, v132, v133
	v_mov_b32_e32 v236, v18
	v_mov_b32_e32 v237, v19
	v_mov_b32_e32 v238, v20
	v_mov_b32_e32 v239, v21
	s_mov_b64 exec, s[34:35]
	global_store_dwordx4 v[138:139], v[18:21], off offset:256
	s_mov_b64 exec, -1
	v_mov_b32_e32 v132, 0
	s_and_b64 vcc, exec, s[0:1]
	v_or_b32_e32 v20, 48, v162
	v_mov_b64_e32 v[18:19], s[12:13]
	v_mad_i64_i32 v[18:19], s[28:29], v20, s66, v[18:19]
	v_lshl_add_u64 v[18:19], s[26:27], 1, v[18:19]
	v_lshl_add_u64 v[18:19], v[18:19], 0, v[0:1]
	global_load_dwordx4 v[26:29], v[18:19], off
	v_ashrrev_i32_e32 v21, 31, v20
	v_lshlrev_b64 v[20:21], 11, v[20:21]
	v_lshl_add_u64 v[134:135], s[10:11], 0, v[20:21]
	v_mov_b32_e32 v138, 0
	v_mov_b32_e32 v139, 0
	v_mov_b32_e32 v136, 0
	v_mov_b32_e32 v137, 0
	s_cbranch_vccnz .LBB0_816
	v_lshl_add_u64 v[20:21], v[134:135], 0, v[0:1]
	v_mov_b32_e32 v138, v218
	v_mov_b32_e32 v139, v219
	v_mov_b32_e32 v136, v242
	v_mov_b32_e32 v137, v243
.LBB0_816:
	s_nop 0
	global_load_dwordx4 v[18:21], v[18:19], off offset:256
	s_and_b64 vcc, exec, s[0:1]
	v_mov_b32_e32 v133, 0
	v_mov_b32_e32 v130, 0
	v_mov_b32_e32 v131, 0
	s_cbranch_vccnz .LBB0_818
	v_lshl_add_u64 v[130:131], v[134:135], 0, v[0:1]
	v_mov_b32_e32 v132, v244
	v_mov_b32_e32 v133, v245
	s_nop 0
	v_mov_b32_e32 v130, v211
	v_mov_b32_e32 v131, v212
.LBB0_818:
	v_add_f32_e32 v126, v126, v14
	v_add_f32_e32 v127, v127, v15
	v_mul_f32_e32 v126, 0xbfb8aa3b, v126
	v_mul_f32_e32 v127, 0xbfb8aa3b, v127
	v_exp_f32_e32 v126, v126
	v_exp_f32_e32 v127, v127
	s_waitcnt vmcnt(5)
	v_lshlrev_b32_e32 v140, 16, v30
	v_and_b32_e32 v141, 0xffff0000, v30
	v_add_f32_e32 v30, v128, v16
	v_mul_f32_e32 v30, 0xbfb8aa3b, v30
	v_add_f32_e32 v128, v129, v17
	v_add_f32_e32 v126, 1.0, v126
	v_add_f32_e32 v127, 1.0, v127
	v_exp_f32_e32 v30, v30
	v_mul_f32_e32 v128, 0xbfb8aa3b, v128
	v_rcp_f32_e32 v126, v126
	v_rcp_f32_e32 v127, v127
	v_exp_f32_e32 v129, v128
	v_add_f32_e32 v122, v122, v10
	v_lshlrev_b32_e32 v142, 16, v154
	v_and_b32_e32 v143, 0xffff0000, v154
	v_add_f32_e32 v30, 1.0, v30
	v_mul_f32_e32 v122, 0xbfb8aa3b, v122
	v_pk_fma_f32 v[126:127], v[126:127], v[140:141], v[142:143]
	v_rcp_f32_e32 v128, v30
	v_add_f32_e32 v30, 1.0, v129
	v_exp_f32_e32 v142, v122
	v_add_f32_e32 v122, v123, v11
	v_rcp_f32_e32 v129, v30
	v_mul_f32_e32 v122, 0xbfb8aa3b, v122
	v_exp_f32_e32 v143, v122
	v_lshlrev_b32_e32 v30, 16, v31
	v_and_b32_e32 v31, 0xffff0000, v31
	v_lshlrev_b32_e32 v140, 16, v155
	v_and_b32_e32 v141, 0xffff0000, v155
	v_pk_fma_f32 v[122:123], v[128:129], v[30:31], v[140:141]
	v_lshlrev_b32_e32 v128, 16, v32
	v_and_b32_e32 v129, 0xffff0000, v32
	v_add_f32_e32 v32, v124, v12
	v_add_f32_e32 v124, v125, v13
	v_add_f32_e32 v30, 1.0, v142
	v_add_f32_e32 v31, 1.0, v143
	v_mul_f32_e32 v32, 0xbfb8aa3b, v32
	v_mul_f32_e32 v124, 0xbfb8aa3b, v124
	v_rcp_f32_e32 v30, v30
	v_rcp_f32_e32 v31, v31
	v_exp_f32_e32 v32, v32
	v_exp_f32_e32 v142, v124
	v_lshlrev_b32_e32 v140, 16, v152
	v_and_b32_e32 v141, 0xffff0000, v152
	v_pk_fma_f32 v[124:125], v[30:31], v[128:129], v[140:141]
	v_add_f32_e32 v30, 1.0, v32
	v_add_f32_e32 v31, 1.0, v142
	v_rcp_f32_e32 v30, v30
	v_rcp_f32_e32 v31, v31
	v_add_f32_e32 v118, v118, v6
	v_add_f32_e32 v119, v119, v7
	v_lshlrev_b32_e32 v32, 16, v33
	v_and_b32_e32 v33, 0xffff0000, v33
	v_lshlrev_b32_e32 v128, 16, v153
	v_and_b32_e32 v129, 0xffff0000, v153
	v_mul_f32_e32 v118, 0xbfb8aa3b, v118
	v_mul_f32_e32 v119, 0xbfb8aa3b, v119
	v_pk_fma_f32 v[128:129], v[30:31], v[32:33], v[128:129]
	v_exp_f32_e32 v118, v118
	v_exp_f32_e32 v119, v119
	v_cvt_pk_bf16_f32 v30, v126, v127
	v_cvt_pk_bf16_f32 v31, v122, v123
	v_cvt_pk_bf16_f32 v32, v124, v125
	v_cvt_pk_bf16_f32 v33, v128, v129
	v_lshl_add_u64 v[122:123], v[150:151], 0, v[0:1]
	v_mov_b32_e32 v240, v30
	v_mov_b32_e32 v241, v31
	v_mov_b32_e32 v246, v32
	v_mov_b32_e32 v247, v33
	s_mov_b64 exec, s[34:35]
	global_store_dwordx4 v[122:123], v[30:33], off
	s_mov_b64 exec, -1
	v_add_f32_e32 v114, v114, v2
	v_add_f32_e32 v115, v115, v3
	s_waitcnt vmcnt(5)
	v_lshlrev_b32_e32 v32, 16, v22
	v_and_b32_e32 v33, 0xffff0000, v22
	v_add_f32_e32 v22, v120, v8
	v_mul_f32_e32 v22, 0xbfb8aa3b, v22
	v_add_f32_e32 v120, v121, v9
	v_add_f32_e32 v30, 1.0, v118
	v_add_f32_e32 v31, 1.0, v119
	v_exp_f32_e32 v22, v22
	v_mul_f32_e32 v120, 0xbfb8aa3b, v120
	v_rcp_f32_e32 v30, v30
	v_rcp_f32_e32 v31, v31
	v_exp_f32_e32 v120, v120
	v_lshlrev_b32_e32 v118, 16, v148
	v_and_b32_e32 v119, 0xffff0000, v148
	v_add_f32_e32 v22, 1.0, v22
	v_pk_fma_f32 v[30:31], v[30:31], v[32:33], v[118:119]
	v_rcp_f32_e32 v32, v22
	v_add_f32_e32 v22, 1.0, v120
	v_mul_f32_e32 v114, 0xbfb8aa3b, v114
	v_mul_f32_e32 v115, 0xbfb8aa3b, v115
	v_rcp_f32_e32 v33, v22
	v_exp_f32_e32 v114, v114
	v_exp_f32_e32 v115, v115
	v_lshlrev_b32_e32 v22, 16, v23
	v_and_b32_e32 v23, 0xffff0000, v23
	v_lshlrev_b32_e32 v118, 16, v149
	v_and_b32_e32 v119, 0xffff0000, v149
	v_pk_fma_f32 v[32:33], v[32:33], v[22:23], v[118:119]
	v_add_f32_e32 v22, 1.0, v114
	v_add_f32_e32 v23, 1.0, v115
	v_lshlrev_b32_e32 v114, 16, v24
	v_and_b32_e32 v115, 0xffff0000, v24
	v_add_f32_e32 v24, v116, v4
	v_add_f32_e32 v116, v117, v5
	v_mul_f32_e32 v24, 0xbfb8aa3b, v24
	v_mul_f32_e32 v116, 0xbfb8aa3b, v116
	v_rcp_f32_e32 v22, v22
	v_rcp_f32_e32 v23, v23
	v_exp_f32_e32 v24, v24
	v_exp_f32_e32 v116, v116
	v_lshlrev_b32_e32 v118, 16, v146
	v_and_b32_e32 v119, 0xffff0000, v146
	v_pk_fma_f32 v[114:115], v[22:23], v[114:115], v[118:119]
	v_add_f32_e32 v22, 1.0, v24
	v_add_f32_e32 v23, 1.0, v116
	v_rcp_f32_e32 v22, v22
	v_rcp_f32_e32 v23, v23
	v_lshlrev_b32_e32 v24, 16, v25
	v_and_b32_e32 v25, 0xffff0000, v25
	v_lshlrev_b32_e32 v116, 16, v147
	v_and_b32_e32 v117, 0xffff0000, v147
	v_pk_fma_f32 v[116:117], v[22:23], v[24:25], v[116:117]
	v_cvt_pk_bf16_f32 v22, v30, v31
	v_cvt_pk_bf16_f32 v23, v32, v33
	v_cvt_pk_bf16_f32 v24, v114, v115
	v_cvt_pk_bf16_f32 v25, v116, v117
	v_mov_b32_e32 v248, v22
	v_mov_b32_e32 v249, v23
	v_mov_b32_e32 v216, v24
	v_mov_b32_e32 v217, v25
	s_mov_b64 exec, s[34:35]
	global_store_dwordx4 v[122:123], v[22:25], off offset:256
	s_mov_b64 exec, -1
	v_add_u32_e32 v114, 0x80, v162
	v_ashrrev_i32_e32 v115, 31, v114
	v_mov_b64_e32 v[22:23], s[12:13]
	v_mad_i64_i32 v[22:23], s[28:29], v114, s66, v[22:23]
	v_lshl_add_u64 v[22:23], s[26:27], 1, v[22:23]
	v_lshl_add_u64 v[22:23], v[22:23], 0, v[0:1]
	global_load_dwordx4 v[30:33], v[22:23], off
	v_lshlrev_b64 v[24:25], 11, v[114:115]
	v_lshl_add_u64 v[120:121], s[10:11], 0, v[24:25]
	v_mov_b32_e32 v118, 0
	s_and_b64 vcc, exec, s[0:1]
	v_mov_b32_e32 v124, 0
	v_mov_b32_e32 v125, 0
	v_mov_b32_e32 v122, 0
	v_mov_b32_e32 v123, 0
	s_cbranch_vccnz .LBB0_820
	v_lshl_add_u64 v[24:25], v[120:121], 0, v[0:1]
	v_mov_b32_e32 v124, v214
	v_mov_b32_e32 v125, v215
	v_mov_b32_e32 v122, v220
	v_mov_b32_e32 v123, v221
.LBB0_820:
	s_nop 0
	global_load_dwordx4 v[22:25], v[22:23], off offset:256
	s_and_b64 vcc, exec, s[0:1]
	v_mov_b32_e32 v119, 0
	v_mov_b32_e32 v116, 0
	v_mov_b32_e32 v117, 0
	s_cbranch_vccnz .LBB0_822
	v_lshl_add_u64 v[116:117], v[120:121], 0, v[0:1]
	ds_read_b64 v[118:119], v222
	s_waitcnt lgkmcnt(0)
	s_nop 0
	ds_read_b64 v[116:117], v222 offset:8
	s_waitcnt lgkmcnt(0)
.LBB0_822:
	v_add_f32_e32 v110, v110, v14
	v_add_f32_e32 v111, v111, v15
	v_mul_f32_e32 v110, 0xbfb8aa3b, v110
	v_mul_f32_e32 v111, 0xbfb8aa3b, v111
	v_exp_f32_e32 v110, v110
	v_exp_f32_e32 v111, v111
	s_waitcnt vmcnt(5)
	v_lshlrev_b32_e32 v126, 16, v26
	v_and_b32_e32 v127, 0xffff0000, v26
	v_add_f32_e32 v26, v112, v16
	v_mul_f32_e32 v26, 0xbfb8aa3b, v26
	v_add_f32_e32 v112, v113, v17
	v_exp_f32_e32 v26, v26
	v_mul_f32_e32 v112, 0xbfb8aa3b, v112
	v_exp_f32_e32 v113, v112
	v_add_f32_e32 v110, 1.0, v110
	v_add_f32_e32 v111, 1.0, v111
	v_rcp_f32_e32 v110, v110
	v_rcp_f32_e32 v111, v111
	v_add_f32_e32 v106, v106, v10
	v_add_f32_e32 v26, 1.0, v26
	v_mul_f32_e32 v106, 0xbfb8aa3b, v106
	v_rcp_f32_e32 v112, v26
	v_add_f32_e32 v26, 1.0, v113
	v_exp_f32_e32 v115, v106
	v_add_f32_e32 v106, v107, v11
	v_lshlrev_b32_e32 v128, 16, v138
	v_and_b32_e32 v129, 0xffff0000, v138
	v_rcp_f32_e32 v113, v26
	v_mul_f32_e32 v106, 0xbfb8aa3b, v106
	v_pk_fma_f32 v[110:111], v[110:111], v[126:127], v[128:129]
	v_exp_f32_e32 v128, v106
	v_lshlrev_b32_e32 v26, 16, v27
	v_and_b32_e32 v27, 0xffff0000, v27
	v_lshlrev_b32_e32 v126, 16, v139
	v_and_b32_e32 v127, 0xffff0000, v139
	v_pk_fma_f32 v[106:107], v[112:113], v[26:27], v[126:127]
	v_lshlrev_b32_e32 v112, 16, v28
	v_and_b32_e32 v113, 0xffff0000, v28
	v_add_f32_e32 v28, v108, v12
	v_add_f32_e32 v108, v109, v13
	v_add_f32_e32 v26, 1.0, v115
	v_add_f32_e32 v27, 1.0, v128
	v_mul_f32_e32 v28, 0xbfb8aa3b, v28
	v_mul_f32_e32 v108, 0xbfb8aa3b, v108
	v_rcp_f32_e32 v26, v26
	v_rcp_f32_e32 v27, v27
	v_exp_f32_e32 v28, v28
	v_exp_f32_e32 v115, v108
	v_lshlrev_b32_e32 v126, 16, v136
	v_and_b32_e32 v127, 0xffff0000, v136
	v_pk_fma_f32 v[108:109], v[26:27], v[112:113], v[126:127]
	v_add_f32_e32 v26, 1.0, v28
	v_add_f32_e32 v27, 1.0, v115
	v_rcp_f32_e32 v26, v26
	v_rcp_f32_e32 v27, v27
	v_add_f32_e32 v102, v102, v6
	v_add_f32_e32 v103, v103, v7
	v_lshlrev_b32_e32 v28, 16, v29
	v_and_b32_e32 v29, 0xffff0000, v29
	v_lshlrev_b32_e32 v112, 16, v137
	v_and_b32_e32 v113, 0xffff0000, v137
	v_mul_f32_e32 v102, 0xbfb8aa3b, v102
	v_mul_f32_e32 v103, 0xbfb8aa3b, v103
	v_pk_fma_f32 v[112:113], v[26:27], v[28:29], v[112:113]
	v_exp_f32_e32 v102, v102
	v_exp_f32_e32 v103, v103
	v_cvt_pk_bf16_f32 v26, v110, v111
	v_cvt_pk_bf16_f32 v27, v106, v107
	v_cvt_pk_bf16_f32 v28, v108, v109
	v_cvt_pk_bf16_f32 v29, v112, v113
	v_lshl_add_u64 v[106:107], v[134:135], 0, v[0:1]
	v_mov_b32_e32 v218, v26
	v_mov_b32_e32 v219, v27
	v_mov_b32_e32 v242, v28
	v_mov_b32_e32 v243, v29
	s_mov_b64 exec, s[34:35]
	global_store_dwordx4 v[106:107], v[26:29], off
	s_mov_b64 exec, -1
	v_add_f32_e32 v98, v98, v2
	v_add_f32_e32 v99, v99, v3
	s_waitcnt vmcnt(5)
	v_lshlrev_b32_e32 v28, 16, v18
	v_and_b32_e32 v29, 0xffff0000, v18
	v_add_f32_e32 v18, v104, v8
	v_mul_f32_e32 v18, 0xbfb8aa3b, v18
	v_add_f32_e32 v104, v105, v9
	v_add_f32_e32 v26, 1.0, v102
	v_add_f32_e32 v27, 1.0, v103
	v_exp_f32_e32 v18, v18
	v_mul_f32_e32 v104, 0xbfb8aa3b, v104
	v_rcp_f32_e32 v26, v26
	v_rcp_f32_e32 v27, v27
	v_exp_f32_e32 v104, v104
	v_lshlrev_b32_e32 v102, 16, v132
	v_and_b32_e32 v103, 0xffff0000, v132
	v_add_f32_e32 v18, 1.0, v18
	v_pk_fma_f32 v[26:27], v[26:27], v[28:29], v[102:103]
	v_rcp_f32_e32 v28, v18
	v_add_f32_e32 v18, 1.0, v104
	v_mul_f32_e32 v98, 0xbfb8aa3b, v98
	v_mul_f32_e32 v99, 0xbfb8aa3b, v99
	v_rcp_f32_e32 v29, v18
	v_exp_f32_e32 v98, v98
	v_exp_f32_e32 v99, v99
	v_lshlrev_b32_e32 v18, 16, v19
	v_and_b32_e32 v19, 0xffff0000, v19
	v_lshlrev_b32_e32 v102, 16, v133
	v_and_b32_e32 v103, 0xffff0000, v133
	v_pk_fma_f32 v[28:29], v[28:29], v[18:19], v[102:103]
	v_add_f32_e32 v18, 1.0, v98
	v_add_f32_e32 v19, 1.0, v99
	v_lshlrev_b32_e32 v98, 16, v20
	v_and_b32_e32 v99, 0xffff0000, v20
	v_add_f32_e32 v20, v100, v4
	v_add_f32_e32 v100, v101, v5
	v_mul_f32_e32 v20, 0xbfb8aa3b, v20
	v_mul_f32_e32 v100, 0xbfb8aa3b, v100
	v_rcp_f32_e32 v18, v18
	v_rcp_f32_e32 v19, v19
	v_exp_f32_e32 v20, v20
	v_exp_f32_e32 v100, v100
	v_lshlrev_b32_e32 v102, 16, v130
	v_and_b32_e32 v103, 0xffff0000, v130
	v_pk_fma_f32 v[98:99], v[18:19], v[98:99], v[102:103]
	v_add_f32_e32 v18, 1.0, v20
	v_add_f32_e32 v19, 1.0, v100
	v_rcp_f32_e32 v18, v18
	v_rcp_f32_e32 v19, v19
	v_lshlrev_b32_e32 v20, 16, v21
	v_and_b32_e32 v21, 0xffff0000, v21
	v_lshlrev_b32_e32 v100, 16, v131
	v_and_b32_e32 v101, 0xffff0000, v131
	v_pk_fma_f32 v[100:101], v[18:19], v[20:21], v[100:101]
	v_cvt_pk_bf16_f32 v18, v26, v27
	v_cvt_pk_bf16_f32 v19, v28, v29
	v_cvt_pk_bf16_f32 v20, v98, v99
	v_cvt_pk_bf16_f32 v21, v100, v101
	v_mov_b32_e32 v244, v18
	v_mov_b32_e32 v245, v19
	v_mov_b32_e32 v211, v20
	v_mov_b32_e32 v212, v21
	s_mov_b64 exec, s[34:35]
	global_store_dwordx4 v[106:107], v[18:21], off offset:256
	s_mov_b64 exec, -1
	v_mov_b32_e32 v100, 0
	s_and_b64 vcc, exec, s[0:1]
	v_or_b32_e32 v20, 16, v114
	v_mov_b64_e32 v[18:19], s[12:13]
	v_mad_i64_i32 v[18:19], s[28:29], v20, s66, v[18:19]
	v_lshl_add_u64 v[18:19], s[26:27], 1, v[18:19]
	v_lshl_add_u64 v[18:19], v[18:19], 0, v[0:1]
	global_load_dwordx4 v[26:29], v[18:19], off
	v_ashrrev_i32_e32 v21, 31, v20
	v_lshlrev_b64 v[20:21], 11, v[20:21]
	v_lshl_add_u64 v[102:103], s[10:11], 0, v[20:21]
	v_mov_b32_e32 v106, 0
	v_mov_b32_e32 v107, 0
	v_mov_b32_e32 v104, 0
	v_mov_b32_e32 v105, 0
	s_cbranch_vccnz .LBB0_824
	v_lshl_add_u64 v[20:21], v[102:103], 0, v[0:1]
	global_load_dwordx2 v[106:107], v[20:21], off sc1
	global_load_dwordx2 v[104:105], v[20:21], off offset:8 sc1

.LBB0_826:
	v_add_f32_e32 v94, v94, v14
	v_add_f32_e32 v95, v95, v15
	v_mul_f32_e32 v94, 0xbfb8aa3b, v94
	v_mul_f32_e32 v95, 0xbfb8aa3b, v95
	v_exp_f32_e32 v94, v94
	v_exp_f32_e32 v95, v95
	s_waitcnt vmcnt(5)
	v_lshlrev_b32_e32 v108, 16, v30
	v_and_b32_e32 v109, 0xffff0000, v30
	v_add_f32_e32 v30, v96, v16
	v_mul_f32_e32 v30, 0xbfb8aa3b, v30
	v_add_f32_e32 v96, v97, v17
	v_add_f32_e32 v94, 1.0, v94
	v_add_f32_e32 v95, 1.0, v95
	v_exp_f32_e32 v30, v30
	v_mul_f32_e32 v96, 0xbfb8aa3b, v96
	v_rcp_f32_e32 v94, v94
	v_rcp_f32_e32 v95, v95
	v_exp_f32_e32 v97, v96
	v_add_f32_e32 v90, v90, v10
	v_lshlrev_b32_e32 v110, 16, v124
	v_and_b32_e32 v111, 0xffff0000, v124
	v_add_f32_e32 v30, 1.0, v30
	v_mul_f32_e32 v90, 0xbfb8aa3b, v90
	v_pk_fma_f32 v[94:95], v[94:95], v[108:109], v[110:111]
	v_rcp_f32_e32 v96, v30
	v_add_f32_e32 v30, 1.0, v97
	v_exp_f32_e32 v110, v90
	v_add_f32_e32 v90, v91, v11
	v_rcp_f32_e32 v97, v30
	v_mul_f32_e32 v90, 0xbfb8aa3b, v90
	v_exp_f32_e32 v111, v90
	v_lshlrev_b32_e32 v30, 16, v31
	v_and_b32_e32 v31, 0xffff0000, v31
	v_lshlrev_b32_e32 v108, 16, v125
	v_and_b32_e32 v109, 0xffff0000, v125
	v_pk_fma_f32 v[90:91], v[96:97], v[30:31], v[108:109]
	v_lshlrev_b32_e32 v96, 16, v32
	v_and_b32_e32 v97, 0xffff0000, v32
	v_add_f32_e32 v32, v92, v12
	v_add_f32_e32 v92, v93, v13
	v_add_f32_e32 v30, 1.0, v110
	v_add_f32_e32 v31, 1.0, v111
	v_mul_f32_e32 v32, 0xbfb8aa3b, v32
	v_mul_f32_e32 v92, 0xbfb8aa3b, v92
	v_rcp_f32_e32 v30, v30
	v_rcp_f32_e32 v31, v31
	v_exp_f32_e32 v32, v32
	v_exp_f32_e32 v110, v92
	v_lshlrev_b32_e32 v108, 16, v122
	v_and_b32_e32 v109, 0xffff0000, v122
	v_pk_fma_f32 v[92:93], v[30:31], v[96:97], v[108:109]
	v_add_f32_e32 v30, 1.0, v32
	v_add_f32_e32 v31, 1.0, v110
	v_rcp_f32_e32 v30, v30
	v_rcp_f32_e32 v31, v31
	v_add_f32_e32 v86, v86, v6
	v_add_f32_e32 v87, v87, v7
	v_lshlrev_b32_e32 v32, 16, v33
	v_and_b32_e32 v33, 0xffff0000, v33
	v_lshlrev_b32_e32 v96, 16, v123
	v_and_b32_e32 v97, 0xffff0000, v123
	v_mul_f32_e32 v86, 0xbfb8aa3b, v86
	v_mul_f32_e32 v87, 0xbfb8aa3b, v87
	v_pk_fma_f32 v[96:97], v[30:31], v[32:33], v[96:97]
	v_exp_f32_e32 v86, v86
	v_exp_f32_e32 v87, v87
	v_cvt_pk_bf16_f32 v30, v94, v95
	v_cvt_pk_bf16_f32 v31, v90, v91
	v_cvt_pk_bf16_f32 v32, v92, v93
	v_cvt_pk_bf16_f32 v33, v96, v97
	v_lshl_add_u64 v[90:91], v[120:121], 0, v[0:1]
	v_mov_b32_e32 v214, v30
	v_mov_b32_e32 v215, v31
	v_mov_b32_e32 v220, v32
	v_mov_b32_e32 v221, v33
	s_mov_b64 exec, s[34:35]
	global_store_dwordx4 v[90:91], v[30:33], off
	s_mov_b64 exec, -1
	v_add_f32_e32 v82, v82, v2
	v_add_f32_e32 v83, v83, v3
	s_waitcnt vmcnt(5)
	v_lshlrev_b32_e32 v32, 16, v22
	v_and_b32_e32 v33, 0xffff0000, v22
	v_add_f32_e32 v22, v88, v8
	v_mul_f32_e32 v22, 0xbfb8aa3b, v22
	v_add_f32_e32 v88, v89, v9
	v_add_f32_e32 v30, 1.0, v86
	v_add_f32_e32 v31, 1.0, v87
	v_exp_f32_e32 v22, v22
	v_mul_f32_e32 v88, 0xbfb8aa3b, v88
	v_rcp_f32_e32 v30, v30
	v_rcp_f32_e32 v31, v31
	v_exp_f32_e32 v88, v88
	v_lshlrev_b32_e32 v86, 16, v118
	v_and_b32_e32 v87, 0xffff0000, v118
	v_add_f32_e32 v22, 1.0, v22
	v_pk_fma_f32 v[30:31], v[30:31], v[32:33], v[86:87]
	v_rcp_f32_e32 v32, v22
	v_add_f32_e32 v22, 1.0, v88
	v_mul_f32_e32 v82, 0xbfb8aa3b, v82
	v_mul_f32_e32 v83, 0xbfb8aa3b, v83
	v_rcp_f32_e32 v33, v22
	v_exp_f32_e32 v82, v82
	v_exp_f32_e32 v83, v83
	v_lshlrev_b32_e32 v22, 16, v23
	v_and_b32_e32 v23, 0xffff0000, v23
	v_lshlrev_b32_e32 v86, 16, v119
	v_and_b32_e32 v87, 0xffff0000, v119
	v_pk_fma_f32 v[32:33], v[32:33], v[22:23], v[86:87]
	v_add_f32_e32 v22, 1.0, v82
	v_add_f32_e32 v23, 1.0, v83
	v_lshlrev_b32_e32 v82, 16, v24
	v_and_b32_e32 v83, 0xffff0000, v24
	v_add_f32_e32 v24, v84, v4
	v_add_f32_e32 v84, v85, v5
	v_mul_f32_e32 v24, 0xbfb8aa3b, v24
	v_mul_f32_e32 v84, 0xbfb8aa3b, v84
	v_rcp_f32_e32 v22, v22
	v_rcp_f32_e32 v23, v23
	v_exp_f32_e32 v24, v24
	v_exp_f32_e32 v84, v84
	v_lshlrev_b32_e32 v86, 16, v116
	v_and_b32_e32 v87, 0xffff0000, v116
	v_pk_fma_f32 v[82:83], v[22:23], v[82:83], v[86:87]
	v_add_f32_e32 v22, 1.0, v24
	v_add_f32_e32 v23, 1.0, v84
	v_rcp_f32_e32 v22, v22
	v_rcp_f32_e32 v23, v23
	v_lshlrev_b32_e32 v24, 16, v25
	v_and_b32_e32 v25, 0xffff0000, v25
	v_lshlrev_b32_e32 v84, 16, v117
	v_and_b32_e32 v85, 0xffff0000, v117
	v_pk_fma_f32 v[84:85], v[22:23], v[24:25], v[84:85]
	v_cvt_pk_bf16_f32 v22, v30, v31
	v_cvt_pk_bf16_f32 v23, v32, v33
	v_cvt_pk_bf16_f32 v24, v82, v83
	v_cvt_pk_bf16_f32 v25, v84, v85
	ds_write_b128 v222, v[22:25]
	s_mov_b64 exec, s[34:35]
	global_store_dwordx4 v[90:91], v[22:25], off offset:256
	s_mov_b64 exec, -1
	v_mov_b32_e32 v84, 0
	s_and_b64 vcc, exec, s[0:1]
	v_or_b32_e32 v24, 32, v114
	v_mov_b64_e32 v[22:23], s[12:13]
	v_mad_i64_i32 v[22:23], s[28:29], v24, s66, v[22:23]
	v_lshl_add_u64 v[22:23], s[26:27], 1, v[22:23]
	v_lshl_add_u64 v[22:23], v[22:23], 0, v[0:1]
	global_load_dwordx4 v[30:33], v[22:23], off
	v_ashrrev_i32_e32 v25, 31, v24
	v_lshlrev_b64 v[24:25], 11, v[24:25]
	v_lshl_add_u64 v[86:87], s[10:11], 0, v[24:25]
	v_mov_b32_e32 v90, 0
	v_mov_b32_e32 v91, 0
	v_mov_b32_e32 v88, 0
	v_mov_b32_e32 v89, 0
	s_cbranch_vccnz .LBB0_828
	v_lshl_add_u64 v[24:25], v[86:87], 0, v[0:1]
	global_load_dwordx2 v[90:91], v[24:25], off sc1
	global_load_dwordx2 v[88:89], v[24:25], off offset:8 sc1

.LBB0_895:
	v_mov_b32_e32 v211, 0x3727c5ac
	v_mov_b32_e32 v212, 0x260
	v_mov_b32_e32 v214, 0x1200
	v_mov_b32_e32 v215, 0xff800000
	v_mov_b32_e32 v220, 0x1680
	v_mov_b32_e32 v221, 0x1b00
	v_mov_b32_e32 v222, 0x1f80
	v_mov_b32_e32 v223, 0x40e00000
	v_readlane_b32 s0, v252, 61
	v_readlane_b32 s1, v252, 62
	s_xor_b64 s[2:3], s[0:1], -1
	s_cmp_le_i32 s90, s14
	s_cselect_b64 s[0:1], -1, 0
	s_and_b64 s[4:5], s[0:1], s[4:5]
	s_andn2_b64 vcc, exec, s[4:5]
	s_cbranch_vccnz .LBB0_922
	v_readlane_b32 s4, v252, 61
	v_readlane_b32 s5, v252, 62
	s_and_b64 s[4:5], s[4:5], exec
	s_mov_b64 s[6:7], s[84:85]
	s_load_dwordx2 s[4:5], s[6:7], 0x100
	s_cselect_b32 s8, 0, 0xf8
	s_add_u32 s8, s6, s8
	s_addc_u32 s9, s7, 0
	s_mov_b64 s[10:11], -1
	s_and_b64 vcc, exec, s[2:3]
	s_cbranch_vccz .LBB0_898
	s_waitcnt lgkmcnt(0)
	s_add_u32 s18, s4, 0x1e00000
	s_addc_u32 s19, s5, 0
	s_mov_b64 s[10:11], 0

.Lgat_nopad:
	s_cmpk_lg_u32 s82, 40
	s_cbranch_scc1 .Lgat_nozero
	s_cmp_lg_u32 s86, 0
	s_cbranch_scc1 .Lgat_nozero
	s_add_u32 s0, s6, 0x16b00000
	s_addc_u32 s1, s7, 0
	v_lshlrev_b32_e32 v2, 4, v213
	v_mov_b32_e32 v4, 0
	v_mov_b32_e32 v5, 0
	v_mov_b32_e32 v6, 0
	v_mov_b32_e32 v7, 0
	global_store_dwordx4 v2, v[4:7], s[0:1]
